# v8 plus nt on all P6 global loads (every P6 input is read once)
# baseline (speedup 1.0000x reference)
.LBB0_765:
	s_ashr_i32 s0, s79, 7
	s_and_b32 s80, s79, 15
	s_ashr_i32 s1, s0, 31
	s_lshl_b64 s[0:1], s[0:1], 11
	s_lshl_b32 s16, s80, 7
	s_ashr_i32 s30, s79, 4
	s_or_b32 s0, s0, s16
	s_and_b32 s18, s30, 7
	s_lshl_b64 s[34:35], s[0:1], 11
	s_add_u32 s19, s3, s34
	s_addc_u32 s31, s52, s35
	s_lshl_b32 s16, s18, 8
	s_add_u32 s34, s19, s16
	s_addc_u32 s35, s31, 0
	s_mul_i32 s19, s1, 0x7000
	s_mul_hi_u32 s31, s0, 0x7000
	s_add_i32 s31, s31, s19
	s_mul_i32 s19, s0, 0x7000
	s_add_u32 s19, s26, s19
	v_lshl_add_u64 v[2:3], s[34:35], 0, v[96:97]
	s_addc_u32 s31, s27, s31
	s_lshl_b32 s18, s18, 9
	v_mov_b32_e32 v211, v230
	v_lshl_add_u64 v[4:5], v[2:3], 0, v[88:89]
	s_add_u32 s34, s19, s18
	v_lshl_add_u64 v[6:7], v[2:3], 0, v[90:91]
	global_load_dwordx4 v[18:21], v[4:5], off nt
	global_load_dwordx4 v[22:25], v[6:7], off nt
	v_lshl_add_u64 v[4:5], v[2:3], 0, v[92:93]
	v_lshl_add_u64 v[2:3], v[2:3], 0, v[94:95]
	s_addc_u32 s35, s31, 0
	global_load_dwordx4 v[26:29], v[4:5], off nt
	global_load_dwordx4 v[30:33], v[2:3], off nt
	v_lshl_add_u64 v[2:3], s[34:35], 0, v[96:97]
	s_add_u32 s81, s0, s66
	v_lshl_add_u64 v[2:3], v[2:3], 0, s[38:39]
	v_mov_b32_e32 v105, v87
	s_addc_u32 s82, s1, 0
	v_lshl_add_u64 v[4:5], v[2:3], 0, v[98:99]
	v_lshl_add_u64 v[6:7], v[2:3], 0, v[100:101]
	v_lshl_add_u64 v[8:9], v[2:3], 0, v[102:103]
	v_lshl_add_u64 v[2:3], v[2:3], 0, v[104:105]
	v_and_or_b32 v166, v211, 15, s81
	v_mov_b32_e32 v167, s82
	global_load_dwordx4 v[34:37], v[4:5], off nt
	global_load_dwordx4 v[38:41], v[4:5], off offset:256 nt
	global_load_dwordx4 v[42:45], v[6:7], off nt
	global_load_dwordx4 v[46:49], v[6:7], off offset:256 nt
	global_load_dwordx4 v[50:53], v[8:9], off nt
	global_load_dwordx4 v[54:57], v[8:9], off offset:256 nt
	global_load_dwordx4 v[58:61], v[2:3], off nt
	global_load_dwordx4 v[62:65], v[2:3], off offset:256 nt
	v_lshlrev_b64 v[2:3], 11, v[166:167]
	v_ashrrev_i32_e32 v212, 4, v211
	v_lshl_add_u64 v[2:3], s[10:11], 0, v[2:3]
	v_lshl_add_u64 v[2:3], v[2:3], 0, s[16:17]
	v_lshlrev_b32_e32 v4, 3, v212
	v_mov_b32_e32 v5, v87
	v_lshl_add_u64 v[14:15], v[4:5], 1, v[2:3]
	global_load_dwordx4 v[2:5], v[14:15], off nt
	global_load_dwordx4 v[6:9], v[14:15], off offset:64 nt
	global_load_dwordx4 v[10:13], v[14:15], off offset:128 nt
	s_nop 0
	global_load_dwordx4 v[14:17], v[14:15], off offset:192 nt
	s_waitcnt vmcnt(15)
	ds_write_b128 v229, v[18:21]
	s_waitcnt vmcnt(14)
	ds_write_b128 v231, v[22:25]
	s_waitcnt vmcnt(13)
	ds_write_b128 v194, v[26:29]
	s_waitcnt vmcnt(12)
	ds_write_b128 v185, v[30:33]
	s_waitcnt vmcnt(11)
	ds_write_b128 v195, v[34:37]
	s_waitcnt vmcnt(9)
	ds_write_b128 v196, v[42:45]
	s_waitcnt vmcnt(7)
	ds_write_b128 v197, v[50:53]
	s_waitcnt vmcnt(5)
	ds_write_b128 v186, v[58:61]
	ds_write_b128 v195, v[38:41] offset:32768
	ds_write_b128 v196, v[46:49] offset:32768
	ds_write_b128 v197, v[54:57] offset:32768
	s_waitcnt vmcnt(4)
	ds_write_b128 v186, v[62:65] offset:32768
	s_and_saveexec_b64 s[44:45], s[6:7]
	s_cbranch_execz .LBB0_772
	s_lshl_b32 s31, s30, 1
	s_sub_i32 s34, 17, s80
	s_add_i32 s35, s80, 2
	s_mov_b64 s[46:47], 0
	v_mov_b64_e32 v[18:19], v[0:1]
	s_branch .LBB0_768
.LBB0_767:
	s_or_b64 exec, exec, s[0:1]
	global_load_dword v20, v[22:23], off nt
	v_cndmask_b32_e32 v21, 0, v199, vcc
	v_lshlrev_b32_e32 v22, 2, v24
	v_lshl_add_u64 v[18:19], v[18:19], 0, s[40:41]
	v_add3_u32 v21, s67, v21, v22
	v_add_u32_e32 v22, 0xfffffe00, v18
	v_cmp_lt_u32_e32 vcc, s71, v22
	s_or_b64 s[46:47], vcc, s[46:47]
	s_waitcnt vmcnt(0)
	ds_write_b32 v21, v20
	s_andn2_b64 exec, exec, s[46:47]
	s_cbranch_execz .LBB0_772

.LBB0_772:
	s_or_b64 exec, exec, s[44:45]
	s_and_saveexec_b64 s[0:1], s[8:9]
	s_cbranch_execz .LBB0_774
	v_or_b32_e32 v18, s16, v0
	v_lshlrev_b32_e32 v18, 2, v18
	global_load_dword v18, v18, s[76:77] nt
	s_waitcnt vmcnt(0)
	ds_write_b32 v182, v18 offset:4096

.LBB0_775:
	v_add_u32_e32 v50, s68, v61
	v_add_u32_e32 v84, v183, v181
	v_add_u32_e32 v218, v50, v58
	ds_write_b128 v188, v[46:49]
	ds_write_b128 v84, v[42:45]
	s_waitcnt lgkmcnt(0)
	s_barrier
	ds_read_b128 v[42:45], v218
	ds_read_b128 v[46:49], v218 offset:4096
	v_add_u32_e32 v109, v50, v60
	ds_read_b128 v[60:63], v109
	ds_read_b128 v[64:67], v109 offset:4096
	s_waitcnt lgkmcnt(3)
	v_mfma_f32_16x16x32_bf16 v[42:45], v[42:45], v[2:5], 0
	v_add_u32_e32 v219, v50, v59
	v_add_u32_e32 v220, v50, v57
	v_lshlrev_b32_e32 v50, 6, v56
	s_waitcnt lgkmcnt(1)
	v_mfma_f32_16x16x32_bf16 v[42:45], v[60:63], v[6:9], v[42:45]
	ds_read_b128 v[58:61], v219
	ds_read_b128 v[68:71], v219 offset:4096
	v_lshlrev_b32_e32 v85, 10, v53
	v_bfe_u32 v190, v52, 1, 1
	s_waitcnt lgkmcnt(1)
	v_mfma_f32_16x16x32_bf16 v[42:45], v[58:61], v[10:13], v[42:45]
	ds_read_b128 v[58:61], v220
	ds_read_b128 v[72:75], v220 offset:4096
	v_and_or_b32 v191, v52, 12, v53
	v_mov_b32_e32 v111, v87
	s_waitcnt lgkmcnt(1)
	v_mfma_f32_16x16x32_bf16 v[42:45], v[58:61], v[14:17], v[42:45]
	ds_read_b128 v[58:61], v218 offset:8192
	v_mov_b32_e32 v113, v87
	v_add_u32_e32 v226, v184, v181
	v_mfma_f32_16x16x32_bf16 v[46:49], v[46:49], v[2:5], 0
	s_nop 3
	v_mul_f32_e64 v44, v180, v44
	v_mul_f32_e64 v45, v180, v45
	v_pk_mul_f32 v[42:43], v[180:181], v[42:43] op_sel_hi:[0,1]
	v_bitop3_b32 v193, v190, v191, 12 bitop3:0x36
	v_mfma_f32_16x16x32_bf16 v[46:49], v[64:67], v[6:9], v[46:49]
	v_lshlrev_b32_e32 v193, 4, v193
	v_max_f32_e64 v107, |v107|, |v107|
	s_xor_b64 s[48:49], s[44:45], -1
	v_mfma_f32_16x16x32_bf16 v[46:49], v[68:71], v[10:13], v[46:49]
	ds_read_b128 v[62:65], v109 offset:8192
	ds_read_b128 v[66:69], v218 offset:12288
	s_mov_b32 s34, 1
	s_mov_b64 s[46:47], -1
	s_waitcnt lgkmcnt(2)
	v_mfma_f32_16x16x32_bf16 v[58:61], v[58:61], v[2:5], 0
	s_waitcnt lgkmcnt(1)
	v_mfma_f32_16x16x32_bf16 v[58:61], v[62:65], v[6:9], v[58:61]
	v_mfma_f32_16x16x32_bf16 v[46:49], v[72:75], v[14:17], v[46:49]
	ds_read_b128 v[70:73], v219 offset:8192
	ds_read_b128 v[74:77], v220 offset:8192
	ds_read_b128 v[78:81], v109 offset:12288
	ds_read_b128 v[62:65], v219 offset:12288
	s_waitcnt lgkmcnt(3)
	v_mfma_f32_16x16x32_bf16 v[56:59], v[70:73], v[10:13], v[58:61]
	ds_read_b128 v[70:73], v220 offset:12288
	s_nop 0
	v_pk_mul_f32 v[48:49], v[180:181], v[48:49] op_sel_hi:[0,1]
	v_pk_mul_f32 v[46:47], v[180:181], v[46:47] op_sel_hi:[0,1]
	v_and_b32_e32 v60, 0x300, v50
	v_lshrrev_b32_e32 v61, 1, v52
	s_waitcnt lgkmcnt(3)
	v_mfma_f32_16x16x32_bf16 v[56:59], v[74:77], v[14:17], v[56:59]
	v_lshlrev_b32_e32 v74, 3, v52
	v_bitop3_b32 v75, v190, v191, 4 bitop3:0x36
	v_mfma_f32_16x16x32_bf16 v[50:53], v[66:69], v[2:5], 0
	v_and_b32_e32 v66, 8, v74
	v_or3_b32 v192, v66, v85, v60
	v_bitop3_b32 v60, v61, v191, 1 bitop3:0x6c
	s_waitcnt lgkmcnt(2)
	v_mfma_f32_16x16x32_bf16 v[50:53], v[78:81], v[6:9], v[50:53]
	v_lshlrev_b32_e32 v60, 4, v60
	v_bitop3_b32 v61, v190, v191, 2 bitop3:0x36
	v_add3_u32 v85, v192, v60, 0
	v_lshlrev_b32_e32 v74, 4, v61
	s_waitcnt lgkmcnt(1)
	v_mfma_f32_16x16x32_bf16 v[50:53], v[62:65], v[10:13], v[50:53]
	ds_read_b64_tr_b16 v[60:61], v85
	ds_read_b64_tr_b16 v[62:63], v85 offset:4096
	v_add3_u32 v221, v74, v192, 0
	v_pk_mul_f32 v[58:59], v[180:181], v[58:59] op_sel_hi:[0,1]
	s_waitcnt lgkmcnt(2)
	v_mfma_f32_16x16x32_bf16 v[64:67], v[70:73], v[14:17], v[50:53]
	s_nop 2
	ds_read_b64_tr_b16 v[50:51], v85 offset:8192
	ds_read_b64_tr_b16 v[52:53], v85 offset:12288
	ds_read_b64_tr_b16 v[68:69], v85 offset:16384
	ds_read_b64_tr_b16 v[70:71], v85 offset:20480
	v_lshlrev_b32_e32 v72, 4, v75
	s_waitcnt lgkmcnt(4)
	v_mfma_f32_16x16x32_bf16 v[42:45], v[60:63], v[18:21], v[42:45]
	ds_read_b64_tr_b16 v[60:61], v85 offset:24576
	ds_read_b64_tr_b16 v[62:63], v85 offset:28672
	v_add3_u32 v222, v72, v192, 0
	v_pk_mul_f32 v[56:57], v[180:181], v[56:57] op_sel_hi:[0,1]
	s_waitcnt lgkmcnt(4)
	v_mfma_f32_16x16x32_bf16 v[42:45], v[50:53], v[22:25], v[42:45]
	ds_read_b64_tr_b16 v[50:51], v221
	ds_read_b64_tr_b16 v[52:53], v221 offset:4096
	v_bitop3_b32 v73, v190, v191, 6 bitop3:0x36
	v_lshlrev_b32_e32 v72, 4, v73
	s_waitcnt lgkmcnt(4)
	v_mfma_f32_16x16x32_bf16 v[42:45], v[68:71], v[26:29], v[42:45]
	ds_read_b64_tr_b16 v[68:69], v221 offset:8192
	ds_read_b64_tr_b16 v[70:71], v221 offset:12288
	v_add3_u32 v225, v72, v192, 0
	v_add3_u32 v223, v193, v192, 0
	s_waitcnt lgkmcnt(2)
	v_mfma_f32_16x16x32_bf16 v[46:49], v[50:53], v[18:21], v[46:49]
	v_mfma_f32_16x16x32_bf16 v[42:45], v[60:63], v[30:33], v[42:45]
	ds_read_b64_tr_b16 v[60:61], v221 offset:16384
	ds_read_b64_tr_b16 v[62:63], v221 offset:20480
	ds_read_b64_tr_b16 v[50:51], v221 offset:24576
	ds_read_b64_tr_b16 v[52:53], v221 offset:28672
	s_waitcnt lgkmcnt(4)
	v_mfma_f32_16x16x32_bf16 v[46:49], v[68:71], v[22:25], v[46:49]
	ds_read_b64_tr_b16 v[68:69], v222
	ds_read_b64_tr_b16 v[70:71], v222 offset:4096
	s_waitcnt lgkmcnt(4)
	v_mfma_f32_16x16x32_bf16 v[46:49], v[60:63], v[26:29], v[46:49]
	ds_read_b64_tr_b16 v[60:61], v222 offset:8192
	ds_read_b64_tr_b16 v[62:63], v222 offset:12288
	s_waitcnt lgkmcnt(2)
	v_mfma_f32_16x16x32_bf16 v[56:59], v[68:71], v[18:21], v[56:59]
	v_mfma_f32_16x16x32_bf16 v[46:49], v[50:53], v[30:33], v[46:49]
	ds_read_b64_tr_b16 v[50:51], v222 offset:16384
	ds_read_b64_tr_b16 v[52:53], v222 offset:20480
	ds_read_b64_tr_b16 v[68:69], v222 offset:24576
	ds_read_b64_tr_b16 v[70:71], v222 offset:28672
	ds_read_b64_tr_b16 v[72:73], v225
	ds_read_b64_tr_b16 v[74:75], v225 offset:4096
	s_waitcnt lgkmcnt(6)
	v_mfma_f32_16x16x32_bf16 v[56:59], v[60:63], v[22:25], v[56:59]
	v_lshl_add_u64 v[62:63], v[54:55], 0, v[110:111]
	v_add_co_u32_e32 v60, vcc, s74, v62
	s_waitcnt lgkmcnt(4)
	v_mfma_f32_16x16x32_bf16 v[50:53], v[50:53], v[26:29], v[56:59]
	v_addc_co_u32_e32 v61, vcc, 0, v63, vcc
	s_nop 2
	v_pk_mul_f32 v[58:59], v[180:181], v[66:67] op_sel_hi:[0,1]
	v_pk_mul_f32 v[56:57], v[180:181], v[64:65] op_sel_hi:[0,1]
	ds_read_b64_tr_b16 v[64:65], v225 offset:8192
	ds_read_b64_tr_b16 v[66:67], v225 offset:12288
	s_waitcnt lgkmcnt(2)
	v_mfma_f32_16x16x32_bf16 v[56:59], v[72:75], v[18:21], v[56:59]
	v_mfma_f32_16x16x32_bf16 v[50:53], v[68:71], v[30:33], v[50:53]
	ds_read_b64_tr_b16 v[68:69], v225 offset:16384
	ds_read_b64_tr_b16 v[70:71], v225 offset:20480
	ds_read_b64_tr_b16 v[74:75], v225 offset:24576
	ds_read_b64_tr_b16 v[76:77], v225 offset:28672
	s_waitcnt lgkmcnt(4)
	v_mfma_f32_16x16x32_bf16 v[56:59], v[64:67], v[22:25], v[56:59]
	v_lshl_add_u64 v[64:65], v[54:55], 0, v[112:113]
	v_bitop3_b32 v113, v190, v191, 10 bitop3:0x36
	v_lshlrev_b32_e32 v113, 4, v113
	s_waitcnt lgkmcnt(2)
	v_mfma_f32_16x16x32_bf16 v[54:57], v[68:71], v[26:29], v[56:59]
	v_add3_u32 v113, v113, v192, 0
	s_nop 1
	v_add_co_u32_e32 v58, vcc, s74, v64
	s_waitcnt lgkmcnt(0)
	v_mfma_f32_16x16x32_bf16 v[54:57], v[74:77], v[30:33], v[54:57]
	v_addc_co_u32_e32 v59, vcc, 0, v65, vcc
	global_load_dwordx4 v[66:69], v[60:61], off nt
	global_load_dwordx4 v[70:73], v[58:59], off nt
	ds_write_b128 v189, v[34:37]
	ds_write_b128 v226, v[38:41]
	s_waitcnt lgkmcnt(0)
	s_barrier
	ds_read_b128 v[34:37], v218 offset:16384
	ds_read_b128 v[38:41], v218 offset:20480
	s_waitcnt lgkmcnt(1)
	v_mfma_f32_16x16x32_bf16 v[34:37], v[34:37], v[2:5], 0
	ds_read_b128 v[58:61], v109 offset:16384
	ds_read_b128 v[74:77], v109 offset:20480
	v_add_co_u32_e32 v62, vcc, s75, v62
	s_waitcnt lgkmcnt(1)
	v_mfma_f32_16x16x32_bf16 v[34:37], v[58:61], v[6:9], v[34:37]
	ds_read_b128 v[58:61], v219 offset:16384
	ds_read_b128 v[78:81], v219 offset:20480
	v_addc_co_u32_e32 v63, vcc, 0, v63, vcc
	v_mfma_f32_16x16x32_bf16 v[38:41], v[38:41], v[2:5], 0
	v_add_co_u32_e32 v64, vcc, s75, v64
	s_waitcnt lgkmcnt(1)
	v_mfma_f32_16x16x32_bf16 v[34:37], v[58:61], v[10:13], v[34:37]
	ds_read_b128 v[58:61], v220 offset:16384
	ds_read_b128 v[232:235], v220 offset:20480
	v_addc_co_u32_e32 v65, vcc, 0, v65, vcc
	v_mfma_f32_16x16x32_bf16 v[38:41], v[74:77], v[6:9], v[38:41]
	s_waitcnt lgkmcnt(1)
	v_mfma_f32_16x16x32_bf16 v[34:37], v[58:61], v[14:17], v[34:37]
	ds_read_b128 v[58:61], v218 offset:24576
	ds_read_b128 v[74:77], v218 offset:28672
	v_mfma_f32_16x16x32_bf16 v[38:41], v[78:81], v[10:13], v[38:41]
	s_nop 4
	v_mul_f32_e64 v36, v180, v36
	v_mul_f32_e64 v37, v180, v37
	v_pk_mul_f32 v[34:35], v[180:181], v[34:35] op_sel_hi:[0,1]
	s_waitcnt lgkmcnt(2)
	v_mfma_f32_16x16x32_bf16 v[38:41], v[232:235], v[14:17], v[38:41]
	ds_read_b128 v[78:81], v109 offset:24576
	ds_read_b128 v[232:235], v109 offset:28672
	s_waitcnt lgkmcnt(3)
	v_mfma_f32_16x16x32_bf16 v[58:61], v[58:61], v[2:5], 0
	s_nop 3
	v_mul_f32_e64 v40, v180, v40
	v_mul_f32_e64 v41, v180, v41
	v_pk_mul_f32 v[38:39], v[180:181], v[38:39] op_sel_hi:[0,1]
	s_waitcnt lgkmcnt(1)
	v_mfma_f32_16x16x32_bf16 v[58:61], v[78:81], v[6:9], v[58:61]
	ds_read_b128 v[78:81], v219 offset:24576
	ds_read_b128 v[236:239], v219 offset:28672
	s_waitcnt lgkmcnt(1)
	v_mfma_f32_16x16x32_bf16 v[58:61], v[78:81], v[10:13], v[58:61]
	ds_read_b128 v[78:81], v220 offset:24576
	ds_read_b128 v[240:243], v220 offset:28672
	s_waitcnt lgkmcnt(1)
	v_mfma_f32_16x16x32_bf16 v[58:61], v[78:81], v[14:17], v[58:61]
	v_bitop3_b32 v78, v190, v191, 8 bitop3:0x36
	v_lshlrev_b32_e32 v78, 4, v78
	v_add3_u32 v111, v78, v192, 0
	v_mfma_f32_16x16x32_bf16 v[74:77], v[74:77], v[2:5], 0
	ds_read_b64_tr_b16 v[78:79], v111
	ds_read_b64_tr_b16 v[80:81], v111 offset:4096
	s_nop 1
	v_pk_mul_f32 v[60:61], v[180:181], v[60:61] op_sel_hi:[0,1]
	v_pk_mul_f32 v[58:59], v[180:181], v[58:59] op_sel_hi:[0,1]
	v_mfma_f32_16x16x32_bf16 v[74:77], v[232:235], v[6:9], v[74:77]
	ds_read_b64_tr_b16 v[232:233], v111 offset:8192
	ds_read_b64_tr_b16 v[234:235], v111 offset:12288
	v_bitop3_b32 v190, v190, v191, 14 bitop3:0x36
	v_lshlrev_b32_e32 v190, 4, v190
	s_waitcnt lgkmcnt(2)
	v_mfma_f32_16x16x32_bf16 v[34:37], v[78:81], v[18:21], v[34:37]
	ds_read_b64_tr_b16 v[78:79], v111 offset:16384
	ds_read_b64_tr_b16 v[80:81], v111 offset:20480
	v_add3_u32 v224, v190, v192, 0
	s_waitcnt lgkmcnt(2)
	v_mfma_f32_16x16x32_bf16 v[34:37], v[232:235], v[22:25], v[34:37]
	ds_read_b64_tr_b16 v[232:233], v111 offset:24576
	ds_read_b64_tr_b16 v[234:235], v111 offset:28672
	s_waitcnt lgkmcnt(2)
	v_mfma_f32_16x16x32_bf16 v[34:37], v[78:81], v[26:29], v[34:37]
	ds_read_b64_tr_b16 v[78:79], v113
	ds_read_b64_tr_b16 v[80:81], v113 offset:4096
	s_waitcnt lgkmcnt(2)
	v_mfma_f32_16x16x32_bf16 v[34:37], v[232:235], v[30:33], v[34:37]
	ds_read_b64_tr_b16 v[232:233], v113 offset:8192
	ds_read_b64_tr_b16 v[234:235], v113 offset:12288
	s_waitcnt lgkmcnt(2)
	v_mfma_f32_16x16x32_bf16 v[38:41], v[78:81], v[18:21], v[38:41]
	ds_read_b64_tr_b16 v[78:79], v113 offset:16384
	ds_read_b64_tr_b16 v[80:81], v113 offset:20480
	s_waitcnt lgkmcnt(2)
	v_mfma_f32_16x16x32_bf16 v[38:41], v[232:235], v[22:25], v[38:41]
	ds_read_b64_tr_b16 v[232:233], v113 offset:24576
	ds_read_b64_tr_b16 v[234:235], v113 offset:28672
	s_waitcnt lgkmcnt(2)
	v_mfma_f32_16x16x32_bf16 v[38:41], v[78:81], v[26:29], v[38:41]
	ds_read_b64_tr_b16 v[78:79], v223
	ds_read_b64_tr_b16 v[80:81], v223 offset:4096
	s_waitcnt lgkmcnt(2)
	v_mfma_f32_16x16x32_bf16 v[38:41], v[232:235], v[30:33], v[38:41]
	ds_read_b64_tr_b16 v[232:233], v223 offset:8192
	ds_read_b64_tr_b16 v[234:235], v223 offset:12288
	s_waitcnt lgkmcnt(2)
	v_mfma_f32_16x16x32_bf16 v[58:61], v[78:81], v[18:21], v[58:61]
	ds_read_b64_tr_b16 v[78:79], v223 offset:16384
	ds_read_b64_tr_b16 v[80:81], v223 offset:20480
	v_mfma_f32_16x16x32_bf16 v[74:77], v[236:239], v[10:13], v[74:77]
	s_waitcnt lgkmcnt(2)
	v_mfma_f32_16x16x32_bf16 v[58:61], v[232:235], v[22:25], v[58:61]
	ds_read_b64_tr_b16 v[232:233], v223 offset:24576
	ds_read_b64_tr_b16 v[234:235], v223 offset:28672
	v_mfma_f32_16x16x32_bf16 v[74:77], v[240:243], v[14:17], v[74:77]
	s_waitcnt lgkmcnt(2)
	v_mfma_f32_16x16x32_bf16 v[58:61], v[78:81], v[26:29], v[58:61]
	ds_read_b64_tr_b16 v[78:79], v224
	ds_read_b64_tr_b16 v[80:81], v224 offset:4096
	s_nop 3
	v_pk_mul_f32 v[76:77], v[180:181], v[76:77] op_sel_hi:[0,1]
	v_pk_mul_f32 v[74:75], v[180:181], v[74:75] op_sel_hi:[0,1]
	s_waitcnt lgkmcnt(2)
	v_mfma_f32_16x16x32_bf16 v[58:61], v[232:235], v[30:33], v[58:61]
	ds_read_b64_tr_b16 v[232:233], v224 offset:8192
	ds_read_b64_tr_b16 v[234:235], v224 offset:12288
	s_waitcnt lgkmcnt(2)
	v_mfma_f32_16x16x32_bf16 v[74:77], v[78:81], v[18:21], v[74:77]
	ds_read_b64_tr_b16 v[78:79], v224 offset:16384
	ds_read_b64_tr_b16 v[80:81], v224 offset:20480
	s_waitcnt lgkmcnt(2)
	v_mfma_f32_16x16x32_bf16 v[74:77], v[232:235], v[22:25], v[74:77]
	ds_read_b64_tr_b16 v[232:233], v224 offset:24576
	ds_read_b64_tr_b16 v[234:235], v224 offset:28672
	s_waitcnt lgkmcnt(2)
	v_mfma_f32_16x16x32_bf16 v[236:239], v[78:81], v[26:29], v[74:77]
	s_nop 3
	global_load_dwordx4 v[74:77], v[62:63], off nt
	global_load_dwordx4 v[78:81], v[64:65], off nt
	s_waitcnt vmcnt(3)
	ds_write_b128 v188, v[66:69]
	s_waitcnt vmcnt(2)
	ds_write_b128 v84, v[70:73]
	s_waitcnt lgkmcnt(0)
	s_barrier
	ds_read_b128 v[66:69], v218
	ds_read_b128 v[70:73], v218 offset:4096
	v_mfma_f32_16x16x32_bf16 v[62:65], v[232:235], v[30:33], v[236:239]
	ds_read_b128 v[232:235], v109
	s_nop 1
	ds_read_b128 v[236:239], v109 offset:4096
	s_waitcnt lgkmcnt(3)
	v_mfma_f32_16x16x32_bf16 v[66:69], v[66:69], v[2:5], 0
	s_waitcnt lgkmcnt(1)
	v_mfma_f32_16x16x32_bf16 v[66:69], v[232:235], v[6:9], v[66:69]
	ds_read_b128 v[232:235], v219
	ds_read_b128 v[240:243], v219 offset:4096
	v_mfma_f32_16x16x32_bf16 v[70:73], v[70:73], v[2:5], 0
	s_waitcnt lgkmcnt(1)
	v_mfma_f32_16x16x32_bf16 v[66:69], v[232:235], v[10:13], v[66:69]
	ds_read_b128 v[232:235], v220
	ds_read_b128 v[244:247], v220 offset:4096
	v_mfma_f32_16x16x32_bf16 v[70:73], v[236:239], v[6:9], v[70:73]
	s_waitcnt lgkmcnt(1)
	v_mfma_f32_16x16x32_bf16 v[66:69], v[232:235], v[14:17], v[66:69]
	ds_read_b128 v[232:235], v218 offset:8192
	ds_read_b128 v[236:239], v218 offset:12288
	v_mfma_f32_16x16x32_bf16 v[70:73], v[240:243], v[10:13], v[70:73]
	s_nop 4
	v_mul_f32_e64 v68, v180, v68
	v_mul_f32_e64 v69, v180, v69
	v_pk_mul_f32 v[66:67], v[180:181], v[66:67] op_sel_hi:[0,1]
	s_waitcnt lgkmcnt(2)
	v_mfma_f32_16x16x32_bf16 v[70:73], v[244:247], v[14:17], v[70:73]
	ds_read_b128 v[240:243], v109 offset:8192
	ds_read_b128 v[244:247], v109 offset:12288
	s_waitcnt lgkmcnt(3)
	v_mfma_f32_16x16x32_bf16 v[232:235], v[232:235], v[2:5], 0
	s_nop 3
	v_mul_f32_e64 v72, v180, v72
	v_mul_f32_e64 v73, v180, v73
	v_pk_mul_f32 v[70:71], v[180:181], v[70:71] op_sel_hi:[0,1]
	s_waitcnt lgkmcnt(1)
	v_mfma_f32_16x16x32_bf16 v[232:235], v[240:243], v[6:9], v[232:235]
	ds_read_b128 v[240:243], v219 offset:8192
	ds_read_b128 v[248:251], v219 offset:12288
	s_waitcnt lgkmcnt(1)
	v_mfma_f32_16x16x32_bf16 v[232:235], v[240:243], v[10:13], v[232:235]
	ds_read_b128 v[240:243], v220 offset:8192
	ds_read_b128 v[190:193], v220 offset:12288
	v_mfma_f32_16x16x32_bf16 v[236:239], v[236:239], v[2:5], 0
	s_waitcnt lgkmcnt(1)
	v_mfma_f32_16x16x32_bf16 v[232:235], v[240:243], v[14:17], v[232:235]
	ds_read_b64_tr_b16 v[240:241], v85 offset:32768
	ds_read_b64_tr_b16 v[242:243], v85 offset:36864
	v_mfma_f32_16x16x32_bf16 v[236:239], v[244:247], v[6:9], v[236:239]
	ds_read_b64_tr_b16 v[244:245], v85 offset:40960
	ds_read_b64_tr_b16 v[246:247], v85 offset:45056
	s_nop 2
	v_pk_mul_f32 v[234:235], v[180:181], v[234:235] op_sel_hi:[0,1]
	v_pk_mul_f32 v[232:233], v[180:181], v[232:233] op_sel_hi:[0,1]
	v_mfma_f32_16x16x32_bf16 v[236:239], v[248:251], v[10:13], v[236:239]
	s_waitcnt lgkmcnt(2)
	v_mfma_f32_16x16x32_bf16 v[66:69], v[240:243], v[18:21], v[66:69]
	v_mfma_f32_16x16x32_bf16 v[190:193], v[190:193], v[14:17], v[236:239]
	s_nop 4
	ds_read_b64_tr_b16 v[236:237], v85 offset:49152
	ds_read_b64_tr_b16 v[238:239], v85 offset:53248
	ds_read_b64_tr_b16 v[240:241], v85 offset:57344
	ds_read_b64_tr_b16 v[242:243], v85 offset:61440
	v_pk_mul_f32 v[192:193], v[180:181], v[192:193] op_sel_hi:[0,1]
	s_waitcnt lgkmcnt(4)
	v_mfma_f32_16x16x32_bf16 v[66:69], v[244:247], v[22:25], v[66:69]
	ds_read_b64_tr_b16 v[244:245], v221 offset:32768
	ds_read_b64_tr_b16 v[246:247], v221 offset:36864
	v_pk_mul_f32 v[190:191], v[180:181], v[190:191] op_sel_hi:[0,1]
	s_waitcnt lgkmcnt(4)
	v_mfma_f32_16x16x32_bf16 v[66:69], v[236:239], v[26:29], v[66:69]
	ds_read_b64_tr_b16 v[236:237], v221 offset:40960
	ds_read_b64_tr_b16 v[238:239], v221 offset:45056
	s_waitcnt lgkmcnt(2)
	v_mfma_f32_16x16x32_bf16 v[70:73], v[244:247], v[18:21], v[70:73]
	v_add_f32_e32 v244, v82, v83
	v_mfma_f32_16x16x32_bf16 v[66:69], v[240:243], v[30:33], v[66:69]
	ds_read_b64_tr_b16 v[240:241], v221 offset:49152
	ds_read_b64_tr_b16 v[242:243], v221 offset:53248
	ds_read_b64_tr_b16 v[82:83], v221 offset:57344
	ds_read_b64_tr_b16 v[84:85], v221 offset:61440
	v_mul_f32_e32 v221, 0xbfb8aa3b, v244
	s_waitcnt lgkmcnt(4)
	v_mfma_f32_16x16x32_bf16 v[70:73], v[236:239], v[22:25], v[70:73]
	ds_read_b64_tr_b16 v[236:237], v222 offset:32768
	ds_read_b64_tr_b16 v[238:239], v222 offset:36864
	v_exp_f32_e32 v221, v221
	s_waitcnt lgkmcnt(4)
	v_mfma_f32_16x16x32_bf16 v[70:73], v[240:243], v[26:29], v[70:73]
	ds_read_b64_tr_b16 v[240:241], v222 offset:40960
	ds_read_b64_tr_b16 v[242:243], v222 offset:45056
	v_max_f32_e32 v107, v107, v221
	v_div_scale_f32 v221, s[44:45], v107, v107, 1.0
	s_waitcnt lgkmcnt(2)
	v_mfma_f32_16x16x32_bf16 v[232:235], v[236:239], v[18:21], v[232:235]
	s_mov_b64 s[44:45], 0
	v_mfma_f32_16x16x32_bf16 v[70:73], v[82:85], v[30:33], v[70:73]
	ds_read_b64_tr_b16 v[82:83], v222 offset:49152
	ds_read_b64_tr_b16 v[84:85], v222 offset:53248
	ds_read_b64_tr_b16 v[236:237], v222 offset:57344
	ds_read_b64_tr_b16 v[238:239], v222 offset:61440
	v_rcp_f32_e32 v222, v221
	s_waitcnt lgkmcnt(4)
	v_mfma_f32_16x16x32_bf16 v[232:235], v[240:243], v[22:25], v[232:235]
	ds_read_b64_tr_b16 v[240:241], v225 offset:32768
	ds_read_b64_tr_b16 v[242:243], v225 offset:36864
	s_waitcnt lgkmcnt(4)
	v_mfma_f32_16x16x32_bf16 v[82:85], v[82:85], v[26:29], v[232:235]
	s_nop 3
	ds_read_b64_tr_b16 v[232:233], v225 offset:40960
	ds_read_b64_tr_b16 v[234:235], v225 offset:45056
	s_waitcnt lgkmcnt(4)
	v_mfma_f32_16x16x32_bf16 v[82:85], v[236:239], v[30:33], v[82:85]
	ds_read_b64_tr_b16 v[236:237], v225 offset:49152
	ds_read_b64_tr_b16 v[238:239], v225 offset:53248
	ds_read_b64_tr_b16 v[244:245], v225 offset:57344
	ds_read_b64_tr_b16 v[246:247], v225 offset:61440
	s_waitcnt vmcnt(1)
	ds_write_b128 v189, v[74:77]
	s_waitcnt vmcnt(0)
	ds_write_b128 v226, v[78:81]
	s_waitcnt lgkmcnt(0)
	v_mfma_f32_16x16x32_bf16 v[190:193], v[240:243], v[18:21], v[190:193]
	s_barrier
	ds_read_b128 v[78:81], v218 offset:16384
	v_mfma_f32_16x16x32_bf16 v[74:77], v[232:235], v[22:25], v[190:193]
	v_div_scale_f32 v225, vcc, 1.0, v107, 1.0
	s_nop 3
	ds_read_b128 v[190:193], v109 offset:16384
	s_waitcnt lgkmcnt(1)
	v_mfma_f32_16x16x32_bf16 v[78:81], v[78:81], v[2:5], 0
	v_mfma_f32_16x16x32_bf16 v[74:77], v[236:239], v[26:29], v[74:77]
	ds_read_b128 v[232:235], v219 offset:16384
	ds_read_b128 v[236:239], v218 offset:20480
	s_waitcnt lgkmcnt(2)
	v_mfma_f32_16x16x32_bf16 v[78:81], v[190:193], v[6:9], v[78:81]
	v_fma_f32 v190, -v221, v222, 1.0
	v_fmac_f32_e32 v222, v190, v222
	v_mul_f32_e32 v226, v225, v222
	v_mfma_f32_16x16x32_bf16 v[74:77], v[244:247], v[30:33], v[74:77]
	ds_read_b128 v[240:243], v220 offset:16384
	ds_read_b128 v[244:247], v109 offset:20480
	ds_read_b128 v[190:193], v219 offset:20480
	s_waitcnt lgkmcnt(4)
	v_mfma_f32_16x16x32_bf16 v[78:81], v[232:235], v[10:13], v[78:81]
	ds_read_b128 v[232:235], v220 offset:20480
	s_waitcnt lgkmcnt(3)
	v_mfma_f32_16x16x32_bf16 v[78:81], v[240:243], v[14:17], v[78:81]
	v_fma_f32 v240, -v221, v226, v225
	v_fmac_f32_e32 v226, v240, v222
	v_fma_f32 v221, -v221, v226, v225
	v_div_fmas_f32 v221, v221, v222, v226
	v_div_fixup_f32 v222, v221, v107, 1.0
	v_mfma_f32_16x16x32_bf16 v[236:239], v[236:239], v[2:5], 0
	v_fma_f32 v178, v222, v44, v178
	v_fma_f32 v179, v222, v45, v179
	v_pk_fma_f32 v[176:177], v[222:223], v[42:43], v[176:177] op_sel_hi:[0,1,1]
	ds_read_b128 v[42:45], v218 offset:24576
	s_waitcnt lgkmcnt(3)
	v_mfma_f32_16x16x32_bf16 v[236:239], v[244:247], v[6:9], v[236:239]
	v_fma_f32 v172, v222, v48, v172
	v_fma_f32 v173, v222, v49, v173
	v_pk_fma_f32 v[174:175], v[222:223], v[46:47], v[174:175] op_sel_hi:[0,1,1]
	ds_read_b128 v[46:49], v109 offset:24576
	s_waitcnt lgkmcnt(3)
	v_mfma_f32_16x16x32_bf16 v[190:193], v[190:193], v[10:13], v[236:239]
	v_fma_f32 v168, v222, v52, v168
	v_fma_f32 v169, v222, v53, v169
	v_pk_fma_f32 v[170:171], v[222:223], v[50:51], v[170:171] op_sel_hi:[0,1,1]
	v_pk_fma_f32 v[154:155], v[222:223], v[40:41], v[154:155] op_sel_hi:[0,1,1]
	s_waitcnt lgkmcnt(1)
	v_mfma_f32_16x16x32_bf16 v[42:45], v[42:45], v[2:5], 0
	v_fma_f32 v156, v222, v38, v156
	v_fma_f32 v157, v222, v39, v157
	v_pk_fma_f32 v[158:159], v[222:223], v[36:37], v[158:159] op_sel_hi:[0,1,1]
	v_pk_fma_f32 v[160:161], v[222:223], v[34:35], v[160:161] op_sel_hi:[0,1,1]
	v_mfma_f32_16x16x32_bf16 v[190:193], v[232:235], v[14:17], v[190:193]
	ds_read_b128 v[232:235], v219 offset:24576
	ds_read_b128 v[236:239], v218 offset:28672
	ds_read_b128 v[50:53], v220 offset:24576
	ds_read_b128 v[240:243], v109 offset:28672
	ds_read_b128 v[34:37], v220 offset:28672
	s_waitcnt lgkmcnt(5)
	v_mfma_f32_16x16x32_bf16 v[42:45], v[46:49], v[6:9], v[42:45]
	ds_read_b128 v[46:49], v219 offset:28672
	v_pk_fma_f32 v[162:163], v[222:223], v[56:57], v[162:163] op_sel_hi:[0,1,1]
	v_pk_fma_f32 v[164:165], v[222:223], v[54:55], v[164:165] op_sel_hi:[0,1,1]
	s_waitcnt lgkmcnt(5)
	v_mfma_f32_16x16x32_bf16 v[42:45], v[232:235], v[10:13], v[42:45]
	v_fma_f32 v150, v222, v60, v150
	v_fma_f32 v151, v222, v61, v151
	v_pk_fma_f32 v[152:153], v[222:223], v[58:59], v[152:153] op_sel_hi:[0,1,1]
	v_pk_fma_f32 v[146:147], v[222:223], v[64:65], v[146:147] op_sel_hi:[0,1,1]
	s_waitcnt lgkmcnt(4)
	v_mfma_f32_16x16x32_bf16 v[38:41], v[236:239], v[2:5], 0
	v_fma_f32 v148, v222, v62, v148
	v_fma_f32 v149, v222, v63, v149
	v_pk_fma_f32 v[142:143], v[222:223], v[68:69], v[142:143] op_sel_hi:[0,1,1]
	v_pk_fma_f32 v[144:145], v[222:223], v[66:67], v[144:145] op_sel_hi:[0,1,1]
	s_waitcnt lgkmcnt(3)
	v_mfma_f32_16x16x32_bf16 v[42:45], v[50:53], v[14:17], v[42:45]
	ds_read_b64_tr_b16 v[50:51], v111 offset:32768
	ds_read_b64_tr_b16 v[52:53], v111 offset:36864
	ds_read_b64_tr_b16 v[54:55], v111 offset:40960
	ds_read_b64_tr_b16 v[56:57], v111 offset:45056
	v_pk_fma_f32 v[138:139], v[222:223], v[72:73], v[138:139] op_sel_hi:[0,1,1]
	s_waitcnt lgkmcnt(6)
	v_mfma_f32_16x16x32_bf16 v[38:41], v[240:243], v[6:9], v[38:41]
	s_nop 0
	v_mul_f32_e64 v44, v180, v44
	v_mul_f32_e64 v45, v180, v45
	v_pk_mul_f32 v[42:43], v[180:181], v[42:43] op_sel_hi:[0,1]
	v_pk_fma_f32 v[140:141], v[222:223], v[70:71], v[140:141] op_sel_hi:[0,1,1]
	s_waitcnt lgkmcnt(4)
	v_mfma_f32_16x16x32_bf16 v[38:41], v[46:49], v[10:13], v[38:41]
	v_mul_f32_e64 v48, v180, v80
	v_mul_f32_e64 v49, v180, v81
	v_pk_mul_f32 v[46:47], v[180:181], v[78:79] op_sel_hi:[0,1]
	v_pk_fma_f32 v[134:135], v[222:223], v[84:85], v[134:135] op_sel_hi:[0,1,1]
	v_mfma_f32_16x16x32_bf16 v[34:37], v[34:37], v[14:17], v[38:41]
	s_nop 2
	ds_read_b64_tr_b16 v[38:39], v111 offset:49152
	ds_read_b64_tr_b16 v[40:41], v111 offset:53248
	v_pk_fma_f32 v[136:137], v[222:223], v[82:83], v[136:137] op_sel_hi:[0,1,1]
	v_pk_fma_f32 v[130:131], v[222:223], v[76:77], v[130:131] op_sel_hi:[0,1,1]
	s_waitcnt lgkmcnt(4)
	v_mfma_f32_16x16x32_bf16 v[46:49], v[50:53], v[18:21], v[46:49]
	ds_read_b64_tr_b16 v[50:51], v111 offset:57344
	ds_read_b64_tr_b16 v[52:53], v111 offset:61440
	v_pk_mul_f32 v[36:37], v[180:181], v[36:37] op_sel_hi:[0,1]
	v_pk_mul_f32 v[34:35], v[180:181], v[34:35] op_sel_hi:[0,1]
	s_waitcnt lgkmcnt(4)
	v_mfma_f32_16x16x32_bf16 v[46:49], v[54:57], v[22:25], v[46:49]
	ds_read_b64_tr_b16 v[54:55], v113 offset:32768
	ds_read_b64_tr_b16 v[56:57], v113 offset:36864
	ds_read_b64_tr_b16 v[58:59], v113 offset:40960
	ds_read_b64_tr_b16 v[60:61], v113 offset:45056
	v_pk_fma_f32 v[132:133], v[222:223], v[74:75], v[132:133] op_sel_hi:[0,1,1]
	s_waitcnt lgkmcnt(6)
	v_mfma_f32_16x16x32_bf16 v[38:41], v[38:41], v[26:29], v[46:49]
	s_and_b64 vcc, exec, s[48:49]
	s_nop 1
	v_pk_mul_f32 v[48:49], v[180:181], v[192:193] op_sel_hi:[0,1]
	v_pk_mul_f32 v[46:47], v[180:181], v[190:191] op_sel_hi:[0,1]
	s_waitcnt lgkmcnt(4)
	v_mfma_f32_16x16x32_bf16 v[38:41], v[50:53], v[30:33], v[38:41]
	ds_read_b64_tr_b16 v[50:51], v113 offset:49152
	ds_read_b64_tr_b16 v[52:53], v113 offset:53248
	s_waitcnt lgkmcnt(4)
	v_mfma_f32_16x16x32_bf16 v[46:49], v[54:57], v[18:21], v[46:49]
	ds_read_b64_tr_b16 v[54:55], v113 offset:57344
	ds_read_b64_tr_b16 v[56:57], v113 offset:61440
	s_nop 1
	v_pk_fma_f32 v[126:127], v[222:223], v[40:41], v[126:127] op_sel_hi:[0,1,1]
	v_pk_fma_f32 v[128:129], v[222:223], v[38:39], v[128:129] op_sel_hi:[0,1,1]
	s_waitcnt lgkmcnt(4)
	v_mfma_f32_16x16x32_bf16 v[46:49], v[58:61], v[22:25], v[46:49]
	ds_read_b64_tr_b16 v[58:59], v223 offset:32768
	ds_read_b64_tr_b16 v[60:61], v223 offset:36864
	s_waitcnt lgkmcnt(4)
	v_mfma_f32_16x16x32_bf16 v[46:49], v[50:53], v[26:29], v[46:49]
	ds_read_b64_tr_b16 v[50:51], v223 offset:40960
	ds_read_b64_tr_b16 v[52:53], v223 offset:45056
	s_waitcnt lgkmcnt(2)
	v_mfma_f32_16x16x32_bf16 v[42:45], v[58:61], v[18:21], v[42:45]
	v_mfma_f32_16x16x32_bf16 v[46:49], v[54:57], v[30:33], v[46:49]
	ds_read_b64_tr_b16 v[54:55], v223 offset:49152
	ds_read_b64_tr_b16 v[56:57], v223 offset:53248
	ds_read_b64_tr_b16 v[58:59], v223 offset:57344
	ds_read_b64_tr_b16 v[60:61], v223 offset:61440
	s_waitcnt lgkmcnt(4)
	v_mfma_f32_16x16x32_bf16 v[42:45], v[50:53], v[22:25], v[42:45]
	ds_read_b64_tr_b16 v[50:51], v224 offset:32768
	ds_read_b64_tr_b16 v[52:53], v224 offset:36864
	v_pk_fma_f32 v[122:123], v[222:223], v[48:49], v[122:123] op_sel_hi:[0,1,1]
	v_pk_fma_f32 v[124:125], v[222:223], v[46:47], v[124:125] op_sel_hi:[0,1,1]
	s_waitcnt lgkmcnt(4)
	v_mfma_f32_16x16x32_bf16 v[42:45], v[54:57], v[26:29], v[42:45]
	ds_read_b64_tr_b16 v[54:55], v224 offset:40960
	ds_read_b64_tr_b16 v[56:57], v224 offset:45056
	s_waitcnt lgkmcnt(2)
	v_mfma_f32_16x16x32_bf16 v[18:21], v[50:53], v[18:21], v[34:37]
	v_mfma_f32_16x16x32_bf16 v[42:45], v[58:61], v[30:33], v[42:45]
	ds_read_b64_tr_b16 v[58:59], v224 offset:49152
	ds_read_b64_tr_b16 v[60:61], v224 offset:53248
	ds_read_b64_tr_b16 v[34:35], v224 offset:57344
	ds_read_b64_tr_b16 v[36:37], v224 offset:61440
	s_waitcnt lgkmcnt(4)
	v_mfma_f32_16x16x32_bf16 v[18:21], v[54:57], v[22:25], v[18:21]
	s_nop 1
	v_fma_f32 v118, v222, v44, v118
	v_fma_f32 v119, v222, v45, v119
	v_pk_fma_f32 v[120:121], v[222:223], v[42:43], v[120:121] op_sel_hi:[0,1,1]
	s_waitcnt lgkmcnt(2)
	v_mfma_f32_16x16x32_bf16 v[18:21], v[58:61], v[26:29], v[18:21]
	s_waitcnt lgkmcnt(0)
	v_mfma_f32_16x16x32_bf16 v[18:21], v[34:37], v[30:33], v[18:21]
	s_nop 7
	v_pk_fma_f32 v[114:115], v[222:223], v[20:21], v[114:115] op_sel_hi:[0,1,1]
	v_pk_fma_f32 v[116:117], v[222:223], v[18:19], v[116:117] op_sel_hi:[0,1,1]
	s_cbranch_vccnz .LBB0_764
.LBB0_776:
	s_or_b32 s48, s34, s30
	s_ashr_i32 s49, s48, 31
	s_lshl_b64 s[48:49], s[48:49], 4
	s_and_b64 s[84:85], s[44:45], exec
	s_cselect_b32 s18, s80, s31
	s_or_b32 s18, s48, s18
	s_mul_i32 s19, s18, 0x11000
	s_mul_hi_u32 s18, s18, 0x11000
	s_mul_i32 s35, s49, 0x11000
	s_add_i32 s18, s18, s35
	s_add_u32 s48, s53, s19
	s_addc_u32 s49, s54, s18
	s_lshl_b32 s18, s34, 11
	s_add_i32 s18, s18, 0
	s_add_i32 s18, s18, 0x18000
	v_mov_b32_e32 v52, v230
	v_mov_b32_e32 v18, s18
	v_lshl_add_u64 v[54:55], s[48:49], 0, v[86:87]
	v_mov_b32_e32 v107, v87
	ds_read_b32 v51, v18 offset:1536
	v_lshl_add_u64 v[18:19], v[54:55], 0, v[106:107]
	v_mov_b32_e32 v109, v87
	v_lshl_add_u64 v[20:21], v[54:55], 0, v[108:109]
	global_load_dwordx4 v[46:49], v[18:19], off nt
	global_load_dwordx4 v[42:45], v[20:21], off nt
	v_add_co_u32_e32 v18, vcc, s72, v18
	v_ashrrev_i32_e32 v53, 4, v52
	s_nop 0
	v_addc_co_u32_e32 v19, vcc, 0, v19, vcc
	v_add_co_u32_e32 v20, vcc, s72, v20
	v_and_b32_e32 v56, 15, v52
	s_nop 0
	v_addc_co_u32_e32 v21, vcc, 0, v21, vcc
	global_load_dwordx4 v[34:37], v[18:19], off nt
	global_load_dwordx4 v[38:41], v[20:21], off nt
	v_lshlrev_b32_e32 v18, 2, v52
	v_and_b32_e32 v30, 12, v18
	v_bfe_u32 v31, v52, 2, 2
	v_lshlrev_b32_e32 v61, 8, v56
	v_bitop3_b32 v18, v30, v53, v31 bitop3:0x36
	v_add_u32_e32 v50, s62, v61
	v_lshlrev_b32_e32 v58, 4, v18
	v_add_u32_e32 v33, v50, v58
	ds_read_b128 v[18:21], v33
	v_add_u32_e32 v22, 4, v53
	v_bitop3_b32 v22, v30, v22, v31 bitop3:0x36
	v_lshlrev_b32_e32 v60, 4, v22
	v_add_u32_e32 v64, v50, v60
	ds_read_b128 v[22:25], v64
	v_add_u32_e32 v26, 8, v53
	v_bitop3_b32 v26, v30, v26, v31 bitop3:0x36
	v_lshlrev_b32_e32 v59, 4, v26
	v_or_b32_e32 v32, s66, v56
	v_add_u32_e32 v63, v50, v59
	v_lshl_add_u32 v62, v32, 2, s18
	ds_read_b128 v[26:29], v63
	ds_read_b32 v67, v62 offset:1024
	s_waitcnt vmcnt(7) lgkmcnt(3)
	v_mfma_f32_16x16x32_bf16 v[18:21], v[18:21], v[2:5], 0
	v_add_u32_e32 v57, 12, v53
	v_bitop3_b32 v30, v30, v57, v31 bitop3:0x36
	v_lshlrev_b32_e32 v57, 4, v30
	v_and_b32_e32 v66, -16, v52
	v_add_u32_e32 v65, v50, v57
	ds_read_b128 v[68:71], v65
	s_waitcnt vmcnt(6) lgkmcnt(3)
	v_mfma_f32_16x16x32_bf16 v[18:21], v[22:25], v[6:9], v[18:21]
	v_add_u32_e32 v66, s18, v66
	ds_read_b128 v[22:25], v66 offset:512
	s_waitcnt lgkmcnt(2)
	v_max_f32_e32 v30, v67, v67
	s_waitcnt vmcnt(5)
	v_mfma_f32_16x16x32_bf16 v[18:21], v[26:29], v[10:13], v[18:21]
	v_max_f32_e32 v26, v51, v51
	v_max_f32_e32 v82, v26, v30
	s_waitcnt lgkmcnt(0)
	v_sub_f32_e32 v22, v22, v82
	v_lshlrev_b32_e32 v50, 2, v53
	v_min_f32_e32 v22, 0, v22
	v_cmp_le_i32_e32 vcc, v50, v32
	v_mul_f32_e32 v22, 0x3fb8aa3b, v22
	s_waitcnt vmcnt(4)
	v_mfma_f32_16x16x32_bf16 v[18:21], v[68:71], v[14:17], v[18:21]
	v_cndmask_b32_e64 v26, 0, 1, vcc
	v_exp_f32_e32 v22, v22
	v_cmp_ge_i32_e32 vcc, v50, v32
	v_sub_f32_e32 v23, v23, v82
	v_min_f32_e32 v23, 0, v23
	v_cndmask_b32_e64 v27, 0, 1, vcc
	v_cndmask_b32_e64 v26, v27, v26, s[44:45]
	v_and_b32_e32 v26, 1, v26
	v_mul_f32_e32 v18, v18, v22
	v_cmp_eq_u32_e32 vcc, 1, v26
	v_or_b32_e32 v22, 1, v50
	v_mul_f32_e32 v23, 0x3fb8aa3b, v23
	v_cndmask_b32_e32 v18, 0, v18, vcc
	v_cmp_lt_i32_e32 vcc, v50, v32
	v_exp_f32_e32 v23, v23
	v_sub_f32_e32 v24, v24, v82
	v_cndmask_b32_e64 v26, 0, 1, vcc
	v_cmp_ge_i32_e32 vcc, v22, v32
	v_min_f32_e32 v24, 0, v24
	v_mul_f32_e32 v19, v19, v23
	v_cndmask_b32_e64 v22, 0, 1, vcc
	v_cndmask_b32_e64 v22, v22, v26, s[44:45]
	v_and_b32_e32 v22, 1, v22
	v_cmp_eq_u32_e32 vcc, 1, v22
	v_or_b32_e32 v22, 2, v50
	v_mul_f32_e32 v24, 0x3fb8aa3b, v24
	v_cndmask_b32_e32 v19, 0, v19, vcc
	v_cmp_le_i32_e32 vcc, v22, v32
	v_exp_f32_e32 v24, v24
	v_cvt_pk_bf16_f32 v18, v18, v19
	v_sub_f32_e32 v51, v51, v82
	v_cndmask_b32_e64 v23, 0, 1, vcc
	v_cmp_ge_i32_e32 vcc, v22, v32
	v_mul_f32_e32 v20, v20, v24
	v_sub_f32_e32 v24, v25, v82
	v_cndmask_b32_e64 v22, 0, 1, vcc
	v_cndmask_b32_e64 v22, v22, v23, s[44:45]
	v_and_b32_e32 v22, 1, v22
	v_cmp_eq_u32_e32 vcc, 1, v22
	v_or_b32_e32 v22, 3, v50
	v_min_f32_e32 v24, 0, v24
	v_cndmask_b32_e32 v20, 0, v20, vcc
	v_cmp_le_i32_e32 vcc, v22, v32
	v_mul_f32_e32 v24, 0x3fb8aa3b, v24
	v_exp_f32_e32 v24, v24
	v_cndmask_b32_e64 v23, 0, 1, vcc
	v_cmp_ge_i32_e32 vcc, v22, v32
	v_mul_f32_e32 v51, 0x3fb8aa3b, v51
	v_mul_f32_e32 v21, v21, v24
	v_cndmask_b32_e64 v22, 0, 1, vcc
	v_cndmask_b32_e64 v22, v22, v23, s[44:45]
	v_and_b32_e32 v22, 1, v22
	v_cmp_eq_u32_e32 vcc, 1, v22
	v_exp_f32_e32 v180, v51
	v_and_or_b32 v51, v187, 64, v56
	v_cndmask_b32_e32 v21, 0, v21, vcc
	v_cvt_pk_bf16_f32 v19, v20, v21
	ds_read_b128 v[20:23], v33 offset:4096
	ds_read_b128 v[24:27], v64 offset:4096
	ds_read_b128 v[28:31], v66 offset:576
	s_waitcnt lgkmcnt(2)
	v_mfma_f32_16x16x32_bf16 v[20:23], v[20:23], v[2:5], 0
	ds_read_b128 v[68:71], v63 offset:4096
	v_lshlrev_b32_e32 v51, 2, v51
	s_waitcnt lgkmcnt(2)
	v_mfma_f32_16x16x32_bf16 v[20:23], v[24:27], v[6:9], v[20:23]
	ds_read_b128 v[24:27], v65 offset:4096
	s_waitcnt lgkmcnt(1)
	v_mfma_f32_16x16x32_bf16 v[20:23], v[68:71], v[10:13], v[20:23]
	s_waitcnt lgkmcnt(0)
	v_mfma_f32_16x16x32_bf16 v[20:23], v[24:27], v[14:17], v[20:23]
	v_sub_f32_e32 v26, v28, v82
	v_min_f32_e32 v26, 0, v26
	v_mul_f32_e32 v26, 0x3fb8aa3b, v26
	v_exp_f32_e32 v26, v26
	v_add_u32_e32 v24, 16, v50
	v_cmp_le_i32_e32 vcc, v24, v32
	s_nop 1
	v_mul_f32_e32 v20, v20, v26
	v_cndmask_b32_e64 v25, 0, 1, vcc
	v_cmp_ge_i32_e32 vcc, v24, v32
	v_sub_f32_e32 v26, v29, v82
	v_min_f32_e32 v26, 0, v26
	v_cndmask_b32_e64 v24, 0, 1, vcc
	v_cndmask_b32_e64 v24, v24, v25, s[44:45]
	v_and_b32_e32 v24, 1, v24
	v_mul_f32_e32 v26, 0x3fb8aa3b, v26
	v_cmp_eq_u32_e32 vcc, 1, v24
	v_add_u32_e32 v24, 17, v50
	v_exp_f32_e32 v26, v26
	v_cndmask_b32_e32 v20, 0, v20, vcc
	v_cmp_le_i32_e32 vcc, v24, v32
	v_mul_f32_e32 v21, v21, v26
	s_nop 0
	v_cndmask_b32_e64 v25, 0, 1, vcc
	v_cmp_ge_i32_e32 vcc, v24, v32
	v_sub_f32_e32 v26, v30, v82
	v_min_f32_e32 v26, 0, v26
	v_cndmask_b32_e64 v24, 0, 1, vcc
	v_cndmask_b32_e64 v24, v24, v25, s[44:45]
	v_and_b32_e32 v24, 1, v24
	v_cmp_eq_u32_e32 vcc, 1, v24
	v_add_u32_e32 v24, 18, v50
	v_mul_f32_e32 v26, 0x3fb8aa3b, v26
	v_cndmask_b32_e32 v21, 0, v21, vcc
	v_cmp_le_i32_e32 vcc, v24, v32
	v_exp_f32_e32 v26, v26
	v_cvt_pk_bf16_f32 v20, v20, v21
	s_nop 0
	v_cndmask_b32_e64 v25, 0, 1, vcc
	v_cmp_ge_i32_e32 vcc, v24, v32
	v_mul_f32_e32 v22, v22, v26
	v_sub_f32_e32 v26, v31, v82
	v_cndmask_b32_e64 v24, 0, 1, vcc
	v_cndmask_b32_e64 v24, v24, v25, s[44:45]
	v_and_b32_e32 v24, 1, v24
	v_cmp_eq_u32_e32 vcc, 1, v24
	v_add_u32_e32 v24, 19, v50
	v_min_f32_e32 v26, 0, v26
	v_cndmask_b32_e32 v22, 0, v22, vcc
	v_cmp_le_i32_e32 vcc, v24, v32
	v_mul_f32_e32 v26, 0x3fb8aa3b, v26
	v_exp_f32_e32 v26, v26
	v_cndmask_b32_e64 v25, 0, 1, vcc
	v_cmp_ge_i32_e32 vcc, v24, v32
	v_mul_f32_e32 v23, v23, v26
	s_nop 0
	v_cndmask_b32_e64 v24, 0, 1, vcc
	v_cndmask_b32_e64 v24, v24, v25, s[44:45]
	v_and_b32_e32 v24, 1, v24
	v_cmp_eq_u32_e32 vcc, 1, v24
	s_nop 1
	v_cndmask_b32_e32 v23, 0, v23, vcc
	v_cvt_pk_bf16_f32 v21, v22, v23
	ds_read_b128 v[22:25], v33 offset:8192
	ds_read_b128 v[26:29], v64 offset:8192
	ds_read_b128 v[68:71], v66 offset:640
	s_waitcnt lgkmcnt(2)
	v_mfma_f32_16x16x32_bf16 v[22:25], v[22:25], v[2:5], 0
	ds_read_b128 v[72:75], v63 offset:8192
	s_waitcnt lgkmcnt(2)
	v_mfma_f32_16x16x32_bf16 v[22:25], v[26:29], v[6:9], v[22:25]
	ds_read_b128 v[26:29], v65 offset:8192
	s_waitcnt lgkmcnt(1)
	v_mfma_f32_16x16x32_bf16 v[22:25], v[72:75], v[10:13], v[22:25]
	s_waitcnt lgkmcnt(0)
	v_mfma_f32_16x16x32_bf16 v[22:25], v[26:29], v[14:17], v[22:25]
	v_sub_f32_e32 v28, v68, v82
	v_min_f32_e32 v28, 0, v28
	v_mul_f32_e32 v28, 0x3fb8aa3b, v28
	v_exp_f32_e32 v28, v28
	v_add_u32_e32 v26, 32, v50
	v_cmp_le_i32_e32 vcc, v26, v32
	s_nop 1
	v_mul_f32_e32 v22, v22, v28
	v_cndmask_b32_e64 v27, 0, 1, vcc
	v_cmp_ge_i32_e32 vcc, v26, v32
	v_sub_f32_e32 v28, v69, v82
	v_min_f32_e32 v28, 0, v28
	v_cndmask_b32_e64 v26, 0, 1, vcc
	v_cndmask_b32_e64 v26, v26, v27, s[44:45]
	v_and_b32_e32 v26, 1, v26
	v_mul_f32_e32 v28, 0x3fb8aa3b, v28
	v_cmp_eq_u32_e32 vcc, 1, v26
	v_add_u32_e32 v26, 33, v50
	v_exp_f32_e32 v28, v28
	v_cndmask_b32_e32 v22, 0, v22, vcc
	v_cmp_le_i32_e32 vcc, v26, v32
	v_mul_f32_e32 v23, v23, v28
	s_nop 0
	v_cndmask_b32_e64 v27, 0, 1, vcc
	v_cmp_ge_i32_e32 vcc, v26, v32
	v_sub_f32_e32 v28, v70, v82
	v_min_f32_e32 v28, 0, v28
	v_cndmask_b32_e64 v26, 0, 1, vcc
	v_cndmask_b32_e64 v26, v26, v27, s[44:45]
	v_and_b32_e32 v26, 1, v26
	v_cmp_eq_u32_e32 vcc, 1, v26
	v_add_u32_e32 v26, 34, v50
	v_mul_f32_e32 v28, 0x3fb8aa3b, v28
	v_cndmask_b32_e32 v23, 0, v23, vcc
	v_cmp_le_i32_e32 vcc, v26, v32
	v_exp_f32_e32 v28, v28
	v_cvt_pk_bf16_f32 v22, v22, v23
	s_nop 0
	v_cndmask_b32_e64 v27, 0, 1, vcc
	v_cmp_ge_i32_e32 vcc, v26, v32
	v_mul_f32_e32 v24, v24, v28
	v_sub_f32_e32 v28, v71, v82
	v_cndmask_b32_e64 v26, 0, 1, vcc
	v_cndmask_b32_e64 v26, v26, v27, s[44:45]
	v_and_b32_e32 v26, 1, v26
	v_cmp_eq_u32_e32 vcc, 1, v26
	v_add_u32_e32 v26, 35, v50
	v_min_f32_e32 v28, 0, v28
	v_cndmask_b32_e32 v24, 0, v24, vcc
	v_cmp_le_i32_e32 vcc, v26, v32
	v_mul_f32_e32 v28, 0x3fb8aa3b, v28
	v_exp_f32_e32 v28, v28
	v_cndmask_b32_e64 v27, 0, 1, vcc
	v_cmp_ge_i32_e32 vcc, v26, v32
	v_mul_f32_e32 v25, v25, v28
	s_nop 0
	v_cndmask_b32_e64 v26, 0, 1, vcc
	v_cndmask_b32_e64 v26, v26, v27, s[44:45]
	v_and_b32_e32 v26, 1, v26
	v_cmp_eq_u32_e32 vcc, 1, v26
	s_nop 1
	v_cndmask_b32_e32 v25, 0, v25, vcc
	v_cvt_pk_bf16_f32 v23, v24, v25
	ds_read_b128 v[24:27], v33 offset:12288
	ds_read_b128 v[28:31], v64 offset:12288
	ds_read_b128 v[68:71], v66 offset:704
	s_waitcnt lgkmcnt(2)
	v_mfma_f32_16x16x32_bf16 v[24:27], v[24:27], v[2:5], 0
	ds_read_b128 v[72:75], v63 offset:12288
	s_waitcnt lgkmcnt(2)
	v_mfma_f32_16x16x32_bf16 v[24:27], v[28:31], v[6:9], v[24:27]
	ds_read_b128 v[28:31], v65 offset:12288
	s_waitcnt lgkmcnt(1)
	v_mfma_f32_16x16x32_bf16 v[24:27], v[72:75], v[10:13], v[24:27]
	s_waitcnt lgkmcnt(0)
	v_mfma_f32_16x16x32_bf16 v[24:27], v[28:31], v[14:17], v[24:27]
	v_sub_f32_e32 v30, v68, v82
	v_min_f32_e32 v30, 0, v30
	v_mul_f32_e32 v30, 0x3fb8aa3b, v30
	v_exp_f32_e32 v30, v30
	v_add_u32_e32 v28, 48, v50
	v_cmp_le_i32_e32 vcc, v28, v32
	s_nop 1
	v_mul_f32_e32 v24, v24, v30
	v_cndmask_b32_e64 v29, 0, 1, vcc
	v_cmp_ge_i32_e32 vcc, v28, v32
	v_sub_f32_e32 v30, v69, v82
	v_min_f32_e32 v30, 0, v30
	v_cndmask_b32_e64 v28, 0, 1, vcc
	v_cndmask_b32_e64 v28, v28, v29, s[44:45]
	v_and_b32_e32 v28, 1, v28
	v_mul_f32_e32 v30, 0x3fb8aa3b, v30
	v_cmp_eq_u32_e32 vcc, 1, v28
	v_add_u32_e32 v28, 49, v50
	v_exp_f32_e32 v30, v30
	v_cndmask_b32_e32 v24, 0, v24, vcc
	v_cmp_le_i32_e32 vcc, v28, v32
	v_mul_f32_e32 v25, v25, v30
	s_nop 0
	v_cndmask_b32_e64 v29, 0, 1, vcc
	v_cmp_ge_i32_e32 vcc, v28, v32
	v_sub_f32_e32 v30, v70, v82
	v_min_f32_e32 v30, 0, v30
	v_cndmask_b32_e64 v28, 0, 1, vcc
	v_cndmask_b32_e64 v28, v28, v29, s[44:45]
	v_and_b32_e32 v28, 1, v28
	v_cmp_eq_u32_e32 vcc, 1, v28
	v_add_u32_e32 v28, 50, v50
	v_mul_f32_e32 v30, 0x3fb8aa3b, v30
	v_cndmask_b32_e32 v25, 0, v25, vcc
	v_cmp_le_i32_e32 vcc, v28, v32
	v_exp_f32_e32 v30, v30
	v_cvt_pk_bf16_f32 v24, v24, v25
	s_nop 0
	v_cndmask_b32_e64 v29, 0, 1, vcc
	v_cmp_ge_i32_e32 vcc, v28, v32
	v_mul_f32_e32 v26, v26, v30
	v_sub_f32_e32 v30, v71, v82
	v_cndmask_b32_e64 v28, 0, 1, vcc
	v_cndmask_b32_e64 v28, v28, v29, s[44:45]
	v_and_b32_e32 v28, 1, v28
	v_cmp_eq_u32_e32 vcc, 1, v28
	v_add_u32_e32 v28, 51, v50
	v_min_f32_e32 v30, 0, v30
	v_cndmask_b32_e32 v26, 0, v26, vcc
	v_cmp_le_i32_e32 vcc, v28, v32
	v_mul_f32_e32 v30, 0x3fb8aa3b, v30
	v_exp_f32_e32 v30, v30
	v_cndmask_b32_e64 v29, 0, 1, vcc
	v_cmp_ge_i32_e32 vcc, v28, v32
	v_mul_f32_e32 v27, v27, v30
	s_nop 0
	v_cndmask_b32_e64 v28, 0, 1, vcc
	v_cndmask_b32_e64 v28, v28, v29, s[44:45]
	v_and_b32_e32 v28, 1, v28
	v_cmp_eq_u32_e32 vcc, 1, v28
	v_add_u32_e32 v30, 64, v50
	s_nop 0
	v_cndmask_b32_e32 v27, 0, v27, vcc
	v_cvt_pk_bf16_f32 v25, v26, v27
	ds_read_b128 v[26:29], v33 offset:16384
	ds_read_b128 v[68:71], v64 offset:16384
	ds_read_b128 v[72:75], v66 offset:768
	s_waitcnt lgkmcnt(2)
	v_mfma_f32_16x16x32_bf16 v[26:29], v[26:29], v[2:5], 0
	ds_read_b128 v[76:79], v63 offset:16384
	s_waitcnt lgkmcnt(1)
	v_sub_f32_e32 v67, v72, v82
	v_min_f32_e32 v67, 0, v67
	v_mfma_f32_16x16x32_bf16 v[26:29], v[68:71], v[6:9], v[26:29]
	ds_read_b128 v[68:71], v65 offset:16384
	v_mul_f32_e32 v67, 0x3fb8aa3b, v67
	v_exp_f32_e32 v67, v67
	s_waitcnt lgkmcnt(1)
	v_mfma_f32_16x16x32_bf16 v[26:29], v[76:79], v[10:13], v[26:29]
	v_cmp_le_i32_e32 vcc, v30, v32
	s_waitcnt lgkmcnt(0)
	v_mfma_f32_16x16x32_bf16 v[26:29], v[68:71], v[14:17], v[26:29]
	v_cndmask_b32_e64 v31, 0, 1, vcc
	v_cmp_ge_i32_e32 vcc, v30, v32
	s_nop 1
	v_cndmask_b32_e64 v30, 0, 1, vcc
	s_nop 2
	v_mul_f32_e32 v26, v26, v67
	v_sub_f32_e32 v67, v73, v82
	v_cndmask_b32_e64 v30, v30, v31, s[44:45]
	v_min_f32_e32 v67, 0, v67
	v_and_b32_e32 v30, 1, v30
	v_mul_f32_e32 v67, 0x3fb8aa3b, v67
	v_cmp_eq_u32_e32 vcc, 1, v30
	v_add_u32_e32 v30, 0x41, v50
	v_exp_f32_e32 v67, v67
	v_cndmask_b32_e32 v26, 0, v26, vcc
	v_cmp_le_i32_e32 vcc, v30, v32
	v_mul_f32_e32 v27, v27, v67
	s_nop 0
	v_cndmask_b32_e64 v31, 0, 1, vcc
	v_cmp_ge_i32_e32 vcc, v30, v32
	v_sub_f32_e32 v67, v74, v82
	v_min_f32_e32 v67, 0, v67
	v_cndmask_b32_e64 v30, 0, 1, vcc
	v_cndmask_b32_e64 v30, v30, v31, s[44:45]
	v_and_b32_e32 v30, 1, v30
	v_cmp_eq_u32_e32 vcc, 1, v30
	v_add_u32_e32 v30, 0x42, v50
	v_mul_f32_e32 v67, 0x3fb8aa3b, v67
	v_cndmask_b32_e32 v27, 0, v27, vcc
	v_cmp_le_i32_e32 vcc, v30, v32
	v_exp_f32_e32 v67, v67
	v_cvt_pk_bf16_f32 v26, v26, v27
	s_nop 0
	v_cndmask_b32_e64 v31, 0, 1, vcc
	v_cmp_ge_i32_e32 vcc, v30, v32
	v_mul_f32_e32 v28, v28, v67
	v_sub_f32_e32 v67, v75, v82
	v_cndmask_b32_e64 v30, 0, 1, vcc
	v_cndmask_b32_e64 v30, v30, v31, s[44:45]
	v_and_b32_e32 v30, 1, v30
	v_cmp_eq_u32_e32 vcc, 1, v30
	v_add_u32_e32 v30, 0x43, v50
	v_min_f32_e32 v67, 0, v67
	v_cndmask_b32_e32 v28, 0, v28, vcc
	v_cmp_le_i32_e32 vcc, v30, v32
	v_mul_f32_e32 v67, 0x3fb8aa3b, v67
	v_exp_f32_e32 v67, v67
	v_cndmask_b32_e64 v31, 0, 1, vcc
	v_cmp_ge_i32_e32 vcc, v30, v32
	v_mul_f32_e32 v29, v29, v67
	s_nop 0
	v_cndmask_b32_e64 v30, 0, 1, vcc
	v_cndmask_b32_e64 v30, v30, v31, s[44:45]
	v_and_b32_e32 v30, 1, v30
	v_cmp_eq_u32_e32 vcc, 1, v30
	v_add_u32_e32 v67, 0x50, v50
	s_nop 0
	v_cndmask_b32_e32 v29, 0, v29, vcc
	v_cvt_pk_bf16_f32 v27, v28, v29
	ds_read_b128 v[28:31], v33 offset:20480
	ds_read_b128 v[68:71], v64 offset:20480
	ds_read_b128 v[72:75], v66 offset:832
	s_waitcnt lgkmcnt(2)
	v_mfma_f32_16x16x32_bf16 v[28:31], v[28:31], v[2:5], 0
	ds_read_b128 v[76:79], v63 offset:20480
	v_cmp_le_i32_e32 vcc, v67, v32
	s_waitcnt lgkmcnt(2)
	v_mfma_f32_16x16x32_bf16 v[28:31], v[68:71], v[6:9], v[28:31]
	ds_read_b128 v[68:71], v65 offset:20480
	s_waitcnt lgkmcnt(1)
	v_mfma_f32_16x16x32_bf16 v[28:31], v[76:79], v[10:13], v[28:31]
	s_waitcnt lgkmcnt(0)
	v_mfma_f32_16x16x32_bf16 v[28:31], v[68:71], v[14:17], v[28:31]
	v_sub_f32_e32 v69, v72, v82
	v_min_f32_e32 v69, 0, v69
	v_mul_f32_e32 v69, 0x3fb8aa3b, v69
	v_exp_f32_e32 v69, v69
	v_cndmask_b32_e64 v68, 0, 1, vcc
	v_cmp_ge_i32_e32 vcc, v67, v32
	s_nop 1
	v_mul_f32_e32 v28, v28, v69
	v_cndmask_b32_e64 v67, 0, 1, vcc
	v_sub_f32_e32 v69, v73, v82
	v_cndmask_b32_e64 v67, v67, v68, s[44:45]
	v_min_f32_e32 v69, 0, v69
	v_and_b32_e32 v67, 1, v67
	v_mul_f32_e32 v69, 0x3fb8aa3b, v69
	v_cmp_eq_u32_e32 vcc, 1, v67
	v_add_u32_e32 v67, 0x51, v50
	v_exp_f32_e32 v69, v69
	v_cndmask_b32_e32 v28, 0, v28, vcc
	v_cmp_le_i32_e32 vcc, v67, v32
	v_mul_f32_e32 v29, v29, v69
	s_nop 0
	v_cndmask_b32_e64 v68, 0, 1, vcc
	v_cmp_ge_i32_e32 vcc, v67, v32
	v_sub_f32_e32 v69, v74, v82
	v_min_f32_e32 v69, 0, v69
	v_cndmask_b32_e64 v67, 0, 1, vcc
	v_cndmask_b32_e64 v67, v67, v68, s[44:45]
	v_and_b32_e32 v67, 1, v67
	v_cmp_eq_u32_e32 vcc, 1, v67
	v_add_u32_e32 v67, 0x52, v50
	v_mul_f32_e32 v69, 0x3fb8aa3b, v69
	v_cndmask_b32_e32 v29, 0, v29, vcc
	v_cmp_le_i32_e32 vcc, v67, v32
	v_exp_f32_e32 v69, v69
	v_cvt_pk_bf16_f32 v28, v28, v29
	s_nop 0
	v_cndmask_b32_e64 v68, 0, 1, vcc
	v_cmp_ge_i32_e32 vcc, v67, v32
	v_mul_f32_e32 v30, v30, v69
	v_sub_f32_e32 v69, v75, v82
	v_cndmask_b32_e64 v67, 0, 1, vcc
	v_cndmask_b32_e64 v67, v67, v68, s[44:45]
	v_and_b32_e32 v67, 1, v67
	v_cmp_eq_u32_e32 vcc, 1, v67
	v_add_u32_e32 v67, 0x53, v50
	v_min_f32_e32 v69, 0, v69
	v_cndmask_b32_e32 v30, 0, v30, vcc
	v_cmp_le_i32_e32 vcc, v67, v32
	v_mul_f32_e32 v69, 0x3fb8aa3b, v69
	v_exp_f32_e32 v69, v69
	v_cndmask_b32_e64 v68, 0, 1, vcc
	v_cmp_ge_i32_e32 vcc, v67, v32
	v_mul_f32_e32 v31, v31, v69
	s_nop 0
	v_cndmask_b32_e64 v67, 0, 1, vcc
	v_cndmask_b32_e64 v67, v67, v68, s[44:45]
	v_and_b32_e32 v67, 1, v67
	v_cmp_eq_u32_e32 vcc, 1, v67
	s_nop 1
	v_cndmask_b32_e32 v31, 0, v31, vcc
	v_cvt_pk_bf16_f32 v29, v30, v31
	ds_read_b128 v[68:71], v33 offset:24576
	ds_read_b128 v[72:75], v64 offset:24576
	ds_read_b128 v[76:79], v66 offset:896
	s_waitcnt lgkmcnt(2)
	v_mfma_f32_16x16x32_bf16 v[68:71], v[68:71], v[2:5], 0
	ds_read_b128 v[218:221], v63 offset:24576
	s_waitcnt lgkmcnt(1)
	v_sub_f32_e32 v67, v76, v82
	v_add_u32_e32 v30, 0x60, v50
	v_mfma_f32_16x16x32_bf16 v[68:71], v[72:75], v[6:9], v[68:71]
	ds_read_b128 v[72:75], v65 offset:24576
	v_min_f32_e32 v67, 0, v67
	v_cmp_le_i32_e32 vcc, v30, v32
	s_waitcnt lgkmcnt(1)
	v_mfma_f32_16x16x32_bf16 v[68:71], v[218:221], v[10:13], v[68:71]
	v_mul_f32_e32 v67, 0x3fb8aa3b, v67
	v_cndmask_b32_e64 v31, 0, 1, vcc
	v_exp_f32_e32 v67, v67
	s_waitcnt lgkmcnt(0)
	v_mfma_f32_16x16x32_bf16 v[68:71], v[72:75], v[14:17], v[68:71]
	v_cmp_ge_i32_e32 vcc, v30, v32
	s_nop 1
	v_cndmask_b32_e64 v30, 0, 1, vcc
	v_cndmask_b32_e64 v30, v30, v31, s[44:45]
	v_and_b32_e32 v30, 1, v30
	s_nop 1
	v_mul_f32_e32 v31, v68, v67
	v_cmp_eq_u32_e32 vcc, 1, v30
	v_sub_f32_e32 v68, v77, v82
	v_min_f32_e32 v68, 0, v68
	v_cndmask_b32_e32 v30, 0, v31, vcc
	v_add_u32_e32 v31, 0x61, v50
	v_cmp_le_i32_e32 vcc, v31, v32
	v_mul_f32_e32 v68, 0x3fb8aa3b, v68
	v_exp_f32_e32 v68, v68
	v_cndmask_b32_e64 v67, 0, 1, vcc
	v_cmp_ge_i32_e32 vcc, v31, v32
	s_nop 1
	v_cndmask_b32_e64 v31, 0, 1, vcc
	v_cndmask_b32_e64 v31, v31, v67, s[44:45]
	v_and_b32_e32 v31, 1, v31
	v_mul_f32_e32 v67, v69, v68
	v_cmp_eq_u32_e32 vcc, 1, v31
	v_sub_f32_e32 v69, v78, v82
	v_min_f32_e32 v69, 0, v69
	v_cndmask_b32_e32 v31, 0, v67, vcc
	v_add_u32_e32 v67, 0x62, v50
	v_cmp_le_i32_e32 vcc, v67, v32
	v_mul_f32_e32 v69, 0x3fb8aa3b, v69
	v_exp_f32_e32 v69, v69
	v_cndmask_b32_e64 v68, 0, 1, vcc
	v_cmp_ge_i32_e32 vcc, v67, v32
	v_cvt_pk_bf16_f32 v30, v30, v31
	s_nop 1
	v_cndmask_b32_e64 v67, 0, 1, vcc
	v_cndmask_b32_e64 v67, v67, v68, s[44:45]
	v_and_b32_e32 v67, 1, v67
	v_mul_f32_e32 v68, v70, v69
	v_cmp_eq_u32_e32 vcc, 1, v67
	v_sub_f32_e32 v70, v79, v82
	v_min_f32_e32 v70, 0, v70
	v_cndmask_b32_e32 v67, 0, v68, vcc
	v_add_u32_e32 v68, 0x63, v50
	v_cmp_le_i32_e32 vcc, v68, v32
	v_mul_f32_e32 v70, 0x3fb8aa3b, v70
	v_exp_f32_e32 v70, v70
	v_cndmask_b32_e64 v69, 0, 1, vcc
	v_cmp_ge_i32_e32 vcc, v68, v32
	s_nop 1
	v_cndmask_b32_e64 v68, 0, 1, vcc
	v_cndmask_b32_e64 v68, v68, v69, s[44:45]
	v_and_b32_e32 v68, 1, v68
	v_mul_f32_e32 v69, v71, v70
	v_cmp_eq_u32_e32 vcc, 1, v68
	s_nop 1
	v_cndmask_b32_e32 v68, 0, v69, vcc
	v_cvt_pk_bf16_f32 v31, v67, v68
	ds_read_b128 v[68:71], v33 offset:28672
	ds_read_b128 v[72:75], v64 offset:28672
	ds_read_b128 v[76:79], v66 offset:960
	s_waitcnt lgkmcnt(2)
	v_mfma_f32_16x16x32_bf16 v[66:69], v[68:71], v[2:5], 0
	ds_read_b128 v[218:221], v63 offset:28672
	v_add_u32_e32 v33, 0x70, v50
	v_cmp_le_i32_e32 vcc, v33, v32
	s_waitcnt lgkmcnt(2)
	v_mfma_f32_16x16x32_bf16 v[66:69], v[72:75], v[6:9], v[66:69]
	ds_read_b128 v[70:73], v65 offset:28672
	v_cndmask_b32_e64 v63, 0, 1, vcc
	v_cmp_ge_i32_e32 vcc, v33, v32
	s_waitcnt lgkmcnt(1)
	v_mfma_f32_16x16x32_bf16 v[66:69], v[218:221], v[10:13], v[66:69]
	v_cndmask_b32_e64 v33, 0, 1, vcc
	v_cndmask_b32_e64 v33, v33, v63, s[44:45]
	v_and_b32_e32 v33, 1, v33
	s_waitcnt lgkmcnt(0)
	v_mfma_f32_16x16x32_bf16 v[64:67], v[70:73], v[14:17], v[66:69]
	v_cmp_eq_u32_e32 vcc, 1, v33
	s_nop 1
	v_sub_f32_e32 v68, v76, v82
	v_min_f32_e32 v68, 0, v68
	v_mul_f32_e32 v68, 0x3fb8aa3b, v68
	v_exp_f32_e32 v68, v68
	s_nop 0
	v_mul_f32_e32 v63, v64, v68
	v_sub_f32_e32 v68, v77, v82
	v_cndmask_b32_e32 v33, 0, v63, vcc
	v_add_u32_e32 v63, 0x71, v50
	v_min_f32_e32 v68, 0, v68
	v_cmp_le_i32_e32 vcc, v63, v32
	v_mul_f32_e32 v68, 0x3fb8aa3b, v68
	v_exp_f32_e32 v68, v68
	v_cndmask_b32_e64 v64, 0, 1, vcc
	v_cmp_ge_i32_e32 vcc, v63, v32
	s_nop 1
	v_cndmask_b32_e64 v63, 0, 1, vcc
	v_cndmask_b32_e64 v63, v63, v64, s[44:45]
	v_and_b32_e32 v63, 1, v63
	v_mul_f32_e32 v64, v65, v68
	v_cmp_eq_u32_e32 vcc, 1, v63
	v_sub_f32_e32 v68, v78, v82
	v_min_f32_e32 v68, 0, v68
	v_cndmask_b32_e32 v63, 0, v64, vcc
	v_add_u32_e32 v64, 0x72, v50
	v_cmp_le_i32_e32 vcc, v64, v32
	v_mul_f32_e32 v68, 0x3fb8aa3b, v68
	v_exp_f32_e32 v68, v68
	v_cndmask_b32_e64 v65, 0, 1, vcc
	v_cmp_ge_i32_e32 vcc, v64, v32
	s_nop 1
	v_cndmask_b32_e64 v64, 0, 1, vcc
	v_cndmask_b32_e64 v64, v64, v65, s[44:45]
	v_and_b32_e32 v64, 1, v64
	v_mul_f32_e32 v65, v66, v68
	v_cmp_eq_u32_e32 vcc, 1, v64
	v_sub_f32_e32 v68, v79, v82
	v_min_f32_e32 v68, 0, v68
	v_cndmask_b32_e32 v64, 0, v65, vcc
	v_add_u32_e32 v65, 0x73, v50
	v_cmp_le_i32_e32 vcc, v65, v32
	v_mul_f32_e32 v68, 0x3fb8aa3b, v68
	v_exp_f32_e32 v68, v68
	v_cndmask_b32_e64 v66, 0, 1, vcc
	v_cmp_ge_i32_e32 vcc, v65, v32
	v_mul_f32_e32 v65, v67, v68
	s_nop 0
	v_cndmask_b32_e64 v32, 0, 1, vcc
	v_cndmask_b32_e64 v32, v32, v66, s[44:45]
	v_and_b32_e32 v32, 1, v32
	v_cmp_eq_u32_e32 vcc, 1, v32
	v_cvt_pk_bf16_f32 v32, v33, v63
	s_nop 1
	v_cndmask_b32_e32 v65, 0, v65, vcc
	v_cvt_pk_bf16_f32 v33, v64, v65
	v_lshlrev_b32_e32 v64, 3, v53
	v_mov_b32_e32 v65, v87
	v_lshl_add_u64 v[68:69], v[64:65], 1, s[48:49]
	v_add_co_u32_e32 v64, vcc, s59, v68
	v_lshl_add_u64 v[76:77], v[68:69], 0, s[42:43]
	s_nop 0
	v_addc_co_u32_e32 v65, vcc, 0, v69, vcc
	global_load_dwordx4 v[64:67], v[64:65], off nt
	s_nop 0
	global_load_dwordx4 v[68:71], v[76:77], off offset:64 nt
	global_load_dwordx4 v[72:75], v[76:77], off offset:128 nt
	s_nop 0
	global_load_dwordx4 v[76:79], v[76:77], off offset:192 nt
	v_cmp_eq_u32_e32 vcc, 0, v56
	ds_read_b32 v83, v62
	s_nop 0
	v_cndmask_b32_e32 v63, 0, v200, vcc
	s_waitcnt vmcnt(2)
	v_cndmask_b32_e32 v71, 0, v71, vcc
	v_cndmask_b32_e32 v67, 0, v67, vcc
	v_cndmask_b32_e32 v66, 0, v66, vcc
	v_cndmask_b32_e32 v65, 0, v65, vcc
	v_cndmask_b32_e32 v64, 0, v64, vcc
	v_cndmask_b32_e32 v70, 0, v70, vcc
	v_cndmask_b32_e32 v69, 0, v69, vcc
	v_cndmask_b32_e32 v68, 0, v68, vcc
	v_mfma_f32_16x16x32_bf16 v[64:67], v[64:67], v[2:5], 0
	s_nop 0
	v_mfma_f32_16x16x32_bf16 v[64:67], v[68:71], v[6:9], v[64:67]
	s_waitcnt vmcnt(1)
	v_cndmask_b32_e32 v71, 0, v75, vcc
	v_cndmask_b32_e32 v70, 0, v74, vcc
	v_cndmask_b32_e32 v69, 0, v73, vcc
	v_cndmask_b32_e32 v68, 0, v72, vcc
	s_nop 1
	v_mfma_f32_16x16x32_bf16 v[64:67], v[68:71], v[10:13], v[64:67]
	s_waitcnt vmcnt(0)
	v_cndmask_b32_e32 v71, 0, v79, vcc
	v_cndmask_b32_e32 v70, 0, v78, vcc
	v_cndmask_b32_e32 v69, 0, v77, vcc
	v_cndmask_b32_e32 v68, 0, v76, vcc
	s_andn2_b64 vcc, exec, s[46:47]
	s_nop 0
	v_mfma_f32_16x16x32_bf16 v[64:67], v[68:71], v[14:17], v[64:67]
	v_perm_b32 v68, v63, v63, s73
	v_mov_b32_e32 v69, v68
	v_mov_b32_e32 v70, v68
	v_mov_b32_e32 v71, v68
	s_nop 3
	v_mul_f32_e32 v64, v180, v64
	s_nop 1
	v_mfma_f32_16x16x32_bf16 v[64:67], v[68:71], v[18:21], v[64:67]
	v_mfma_f32_16x16x32_bf16 v[64:67], v[68:71], v[22:25], v[64:67]
	v_mfma_f32_16x16x32_bf16 v[64:67], v[68:71], v[26:29], v[64:67]
	v_mfma_f32_16x16x32_bf16 v[62:65], v[68:71], v[30:33], v[64:67]
	s_nop 7
	ds_bpermute_b32 v107, v51, v62
	s_cbranch_vccnz .LBB0_775
	v_or_b32_e32 v62, s81, v56
	v_mov_b32_e32 v63, s82
	v_lshlrev_b64 v[62:63], 11, v[62:63]
	v_lshl_add_u64 v[62:63], s[0:1], 0, v[62:63]
	v_mov_b32_e32 v51, v87
	v_lshl_add_u64 v[50:51], v[62:63], 0, v[50:51]
	global_load_dword v217, v[50:51], off nt
	global_load_dword v216, v[50:51], off offset:16 nt
	global_load_dword v215, v[50:51], off offset:32 nt
	global_load_dword v214, v[50:51], off offset:48 nt
	global_load_dword v213, v[50:51], off offset:64 nt
	global_load_dword v210, v[50:51], off offset:80 nt
	global_load_dword v209, v[50:51], off offset:96 nt
	global_load_dword v208, v[50:51], off offset:112 nt
	global_load_dword v207, v[50:51], off offset:128 nt
	global_load_dword v206, v[50:51], off offset:144 nt
	global_load_dword v205, v[50:51], off offset:160 nt
	global_load_dword v204, v[50:51], off offset:176 nt
	global_load_dword v203, v[50:51], off offset:192 nt
	global_load_dword v202, v[50:51], off offset:208 nt
	global_load_dword v201, v[50:51], off offset:224 nt
	global_load_dword v105, v[50:51], off offset:240 nt
	s_branch .LBB0_775
